# memory cross-attention tile loop: K and V fragment LDS reads run one MFMA ahead in two alternating register quads (was read -> wait -> MFMA, 16 exposed LDS latencies per tile)
# speedup vs baseline: 1.0118x; 1.0083x over previous
.LBB0_1267:
	s_and_b32 s6, s26, 1
	s_mul_i32 s7, s6, 0x2400
	v_mov_b32_e32 v32, 0
	v_add_u32_e32 v94, s7, v101
	global_load_dwordx4 v[84:87], v[92:93], off offset:-512
	global_load_dwordx4 v[80:83], v[92:93], off
	ds_read_b128 v[104:107], v94
	ds_read_b128 v[108:111], v94 offset:4608
	v_mov_b32_e32 v33, v32
	v_mov_b32_e32 v34, v32
	v_mov_b32_e32 v35, v32
	v_mov_b32_e32 v36, v32
	v_mov_b32_e32 v37, v32
	v_mov_b32_e32 v38, v32
	v_mov_b32_e32 v39, v32
	v_mov_b32_e32 v40, v32
	v_mov_b32_e32 v41, v32
	v_mov_b32_e32 v42, v32
	v_mov_b32_e32 v43, v32
	v_mov_b32_e32 v44, v32
	v_mov_b32_e32 v45, v32
	v_mov_b32_e32 v46, v32
	v_mov_b32_e32 v47, v32
	v_and_b32_e32 v95, 64, v225
	v_add_u32_e32 v95, 64, v95
	s_waitcnt lgkmcnt(1)
	v_mfma_f32_32x32x16_bf16 v[48:63], v[104:107], v[76:79], v[32:47]
	ds_read_b128 v[104:107], v94 offset:32
	s_waitcnt lgkmcnt(1)
	v_mfma_f32_32x32x16_bf16 v[32:47], v[108:111], v[76:79], v[32:47]
	ds_read_b128 v[108:111], v94 offset:4640
	s_waitcnt lgkmcnt(1)
	v_mfma_f32_32x32x16_bf16 v[48:63], v[104:107], v[72:75], v[48:63]
	ds_read_b128 v[104:107], v94 offset:64
	s_waitcnt lgkmcnt(1)
	v_mfma_f32_32x32x16_bf16 v[32:47], v[108:111], v[72:75], v[32:47]
	ds_read_b128 v[108:111], v94 offset:4672
	s_waitcnt lgkmcnt(1)
	v_mfma_f32_32x32x16_bf16 v[48:63], v[104:107], v[68:71], v[48:63]
	ds_read_b128 v[104:107], v94 offset:96
	s_waitcnt lgkmcnt(1)
	v_mfma_f32_32x32x16_bf16 v[32:47], v[108:111], v[68:71], v[32:47]
	ds_read_b128 v[108:111], v94 offset:4704
	v_xor_b32_e32 v94, 32, v225
	v_cmp_lt_i32_e32 vcc, v94, v95
	s_nop 1
	v_cndmask_b32_e32 v94, v225, v94, vcc
	v_lshlrev_b32_e32 v102, 2, v94
	s_waitcnt lgkmcnt(1)
	v_mfma_f32_32x32x16_bf16 v[48:63], v[104:107], v[64:67], v[48:63]
	s_waitcnt lgkmcnt(0)
	v_mfma_f32_32x32x16_bf16 v[32:47], v[108:111], v[64:67], v[32:47]
	s_nop 9
	v_max_f32_e32 v95, v49, v49
	v_max_f32_e32 v99, v48, v48
	v_max_f32_e32 v95, v99, v95
	v_max3_f32 v99, v50, v51, v33
	v_max3_f32 v95, v95, v32, v34
	v_max3_f32 v95, v95, v35, v52
	v_max3_f32 v99, v99, v54, v55
	v_max3_f32 v95, v95, v53, v36
	v_max3_f32 v99, v99, v38, v39
	v_max3_f32 v95, v95, v37, v56
	v_max3_f32 v99, v99, v58, v59
	v_max3_f32 v95, v95, v57, v40
	v_max3_f32 v99, v99, v42, v43
	v_max3_f32 v95, v95, v41, v60
	v_max3_f32 v99, v99, v62, v63
	v_max3_f32 v95, v95, v61, v44
	v_max3_f32 v99, v99, v46, v47
	v_max3_f32 v94, v95, v45, v99
	ds_bpermute_b32 v95, v102, v94
	s_waitcnt lgkmcnt(0)
	v_max_f32_e32 v95, v95, v95
	v_max_f32_e32 v94, v94, v95
	v_mov_b32_e32 v95, v100
	v_add_f32_e32 v94, 0, v94
	v_max_f32_e32 v99, v95, v95
	v_max_f32_e32 v100, v99, v94
	v_sub_f32_e32 v48, v48, v100
	v_sub_f32_e32 v32, v32, v100
	v_sub_f32_e32 v99, v95, v100
	v_exp_f32_e32 v94, v48
	v_exp_f32_e32 v95, v32
	v_sub_f32_e32 v32, v49, v100
	v_sub_f32_e32 v33, v33, v100
	v_exp_f32_e32 v32, v32
	v_exp_f32_e32 v33, v33
	v_sub_f32_e32 v48, v50, v100
	v_sub_f32_e32 v34, v34, v100
	v_exp_f32_e32 v48, v48
	v_exp_f32_e32 v49, v34
	v_sub_f32_e32 v34, v51, v100
	v_sub_f32_e32 v35, v35, v100
	v_exp_f32_e32 v34, v34
	v_exp_f32_e32 v35, v35
	v_pk_add_f32 v[50:51], v[94:95], 0 op_sel_hi:[1,0]
	v_sub_f32_e32 v36, v36, v100
	v_pk_add_f32 v[50:51], v[32:33], v[50:51]
	v_sub_f32_e32 v37, v37, v100
	v_pk_add_f32 v[50:51], v[48:49], v[50:51]
	v_exp_f32_e32 v37, v37
	v_pk_add_f32 v[104:105], v[34:35], v[50:51]
	v_sub_f32_e32 v50, v52, v100
	v_exp_f32_e32 v50, v50
	v_exp_f32_e32 v51, v36
	v_sub_f32_e32 v36, v53, v100
	v_exp_f32_e32 v36, v36
	v_sub_f32_e32 v52, v54, v100
	v_sub_f32_e32 v38, v38, v100
	v_exp_f32_e32 v52, v52
	v_exp_f32_e32 v53, v38
	v_sub_f32_e32 v38, v55, v100
	v_sub_f32_e32 v39, v39, v100
	v_exp_f32_e32 v38, v38
	v_exp_f32_e32 v39, v39
	v_sub_f32_e32 v54, v56, v100
	v_sub_f32_e32 v40, v40, v100
	v_sub_f32_e32 v42, v42, v100
	v_sub_f32_e32 v44, v44, v100
	v_sub_f32_e32 v46, v46, v100
	v_exp_f32_e32 v54, v54
	v_exp_f32_e32 v55, v40
	v_sub_f32_e32 v40, v57, v100
	v_sub_f32_e32 v41, v41, v100
	v_sub_f32_e32 v56, v58, v100
	v_exp_f32_e32 v57, v42
	v_sub_f32_e32 v42, v59, v100
	v_sub_f32_e32 v58, v60, v100
	v_exp_f32_e32 v59, v44
	v_sub_f32_e32 v44, v61, v100
	v_sub_f32_e32 v60, v62, v100
	v_exp_f32_e32 v61, v46
	v_sub_f32_e32 v46, v63, v100
	v_pk_add_f32 v[62:63], v[50:51], v[104:105]
	v_exp_f32_e32 v40, v40
	v_exp_f32_e32 v41, v41
	v_pk_add_f32 v[62:63], v[36:37], v[62:63]
	v_exp_f32_e32 v56, v56
	v_sub_f32_e32 v43, v43, v100
	v_pk_add_f32 v[62:63], v[52:53], v[62:63]
	v_exp_f32_e32 v42, v42
	v_exp_f32_e32 v43, v43
	v_pk_add_f32 v[62:63], v[38:39], v[62:63]
	v_exp_f32_e32 v58, v58
	v_sub_f32_e32 v45, v45, v100
	v_pk_add_f32 v[62:63], v[54:55], v[62:63]
	v_exp_f32_e32 v44, v44
	v_exp_f32_e32 v45, v45
	v_pk_add_f32 v[62:63], v[40:41], v[62:63]
	v_exp_f32_e32 v60, v60
	v_sub_f32_e32 v47, v47, v100
	v_pk_add_f32 v[62:63], v[56:57], v[62:63]
	v_exp_f32_e32 v46, v46
	v_exp_f32_e32 v47, v47
	v_pk_add_f32 v[62:63], v[42:43], v[62:63]
	s_nop 0
	v_pk_add_f32 v[62:63], v[58:59], v[62:63]
	s_nop 0
	v_pk_add_f32 v[62:63], v[44:45], v[62:63]
	s_nop 0
	v_pk_add_f32 v[62:63], v[60:61], v[62:63]
	s_nop 0
	v_pk_add_f32 v[104:105], v[46:47], v[62:63]
	v_exp_f32_e32 v62, v99
	v_add_f32_e32 v63, v104, v105
	ds_bpermute_b32 v99, v102, v63
	v_cmp_neq_f32_e32 vcc, 1.0, v62
	s_cbranch_vccz .LBB0_1269
	ds_write_b32 v98, v62 offset:43008
	ds_read_b128 v[104:107], v97 offset:43104
	ds_read_b128 v[108:111], v97 offset:43072
	ds_read_b128 v[112:115], v97 offset:43040
	ds_read_b128 v[116:119], v97 offset:43008
	s_waitcnt lgkmcnt(3)
	v_pk_mul_f32 v[14:15], v[106:107], v[14:15]
	s_waitcnt lgkmcnt(2)
	v_pk_mul_f32 v[10:11], v[110:111], v[10:11]
	s_waitcnt lgkmcnt(1)
	v_pk_mul_f32 v[6:7], v[114:115], v[6:7]
	s_waitcnt lgkmcnt(0)
	v_pk_mul_f32 v[2:3], v[118:119], v[2:3]
	v_pk_mul_f32 v[12:13], v[104:105], v[12:13]
	v_pk_mul_f32 v[8:9], v[108:109], v[8:9]
	v_pk_mul_f32 v[4:5], v[112:113], v[4:5]
	v_pk_mul_f32 v[0:1], v[116:117], v[0:1]
	v_pk_mul_f32 v[30:31], v[106:107], v[30:31]
	v_pk_mul_f32 v[26:27], v[110:111], v[26:27]
	v_pk_mul_f32 v[22:23], v[114:115], v[22:23]
	v_pk_mul_f32 v[18:19], v[118:119], v[18:19]
	v_pk_mul_f32 v[28:29], v[104:105], v[28:29]
	v_pk_mul_f32 v[24:25], v[108:109], v[24:25]
	v_pk_mul_f32 v[20:21], v[112:113], v[20:21]
	v_pk_mul_f32 v[16:17], v[116:117], v[16:17]
.LBB0_1269:
	s_mulk_i32 s6, 0x3000
	v_cvt_pk_bf16_f32 v110, v58, v44
	v_add_u32_e32 v44, s6, v91
	v_cvt_pk_bf16_f32 v104, v94, v32
	v_cvt_pk_bf16_f32 v105, v48, v34
	v_cvt_pk_bf16_f32 v106, v50, v36
	v_cvt_pk_bf16_f32 v107, v52, v38
	v_cvt_pk_bf16_f32 v108, v54, v40
	v_cvt_pk_bf16_f32 v109, v56, v42
	v_cvt_pk_bf16_f32 v34, v51, v37
	v_cvt_pk_bf16_f32 v36, v55, v41
	v_cvt_pk_bf16_f32 v37, v57, v43
	v_cvt_pk_bf16_f32 v111, v60, v46
	v_cvt_pk_bf16_f32 v32, v95, v33
	v_cvt_pk_bf16_f32 v33, v49, v35
	v_cvt_pk_bf16_f32 v35, v53, v39
	v_cvt_pk_bf16_f32 v38, v59, v45
	v_cvt_pk_bf16_f32 v39, v61, v47
	ds_read_b64_tr_b16 v[40:41], v44 offset:18432
	ds_read_b64_tr_b16 v[42:43], v44 offset:19968
	ds_read_b64_tr_b16 v[48:49], v44 offset:18496
	ds_read_b64_tr_b16 v[50:51], v44 offset:20032
	s_waitcnt lgkmcnt(2)
	v_mfma_f32_32x32x16_bf16 v[0:15], v[104:107], v[40:43], v[0:15]
	ds_read_b64_tr_b16 v[40:41], v44 offset:21504
	ds_read_b64_tr_b16 v[42:43], v44 offset:23040
	s_waitcnt lgkmcnt(2)
	v_mfma_f32_32x32x16_bf16 v[16:31], v[104:107], v[48:51], v[16:31]
	ds_read_b64_tr_b16 v[48:49], v44 offset:21568
	ds_read_b64_tr_b16 v[50:51], v44 offset:23104
	v_add_f32_e32 v99, v63, v99
	s_add_i32 s26, s26, 1
	v_fmac_f32_e32 v99, v103, v62
	s_waitcnt lgkmcnt(2)
	v_mfma_f32_32x32x16_bf16 v[0:15], v[108:111], v[40:43], v[0:15]
	ds_read_b64_tr_b16 v[40:41], v44 offset:24576
	ds_read_b64_tr_b16 v[42:43], v44 offset:26112
	s_waitcnt lgkmcnt(2)
	v_mfma_f32_32x32x16_bf16 v[16:31], v[108:111], v[48:51], v[16:31]
	ds_read_b64_tr_b16 v[48:49], v44 offset:24640
	ds_read_b64_tr_b16 v[50:51], v44 offset:26176
	s_waitcnt lgkmcnt(2)
	v_mfma_f32_32x32x16_bf16 v[0:15], v[32:35], v[40:43], v[0:15]
	ds_read_b64_tr_b16 v[40:41], v44 offset:27648
	ds_read_b64_tr_b16 v[42:43], v44 offset:29184
	s_waitcnt lgkmcnt(2)
	v_mfma_f32_32x32x16_bf16 v[16:31], v[32:35], v[48:51], v[16:31]
	ds_read_b64_tr_b16 v[48:49], v44 offset:27712
	ds_read_b64_tr_b16 v[50:51], v44 offset:29248
	s_waitcnt lgkmcnt(2)
	v_mfma_f32_32x32x16_bf16 v[0:15], v[36:39], v[40:43], v[0:15]
	s_waitcnt lgkmcnt(0)
	v_mfma_f32_32x32x16_bf16 v[16:31], v[36:39], v[48:51], v[16:31]
	s_bitcmp1_b32 s26, 0
	s_cselect_b32 s6, 0x2400, 0
	v_add_u32_e32 v32, s6, v88
	s_cselect_b32 s6, 0x3000, 0
	s_waitcnt vmcnt(1)
	ds_write_b128 v32, v[84:87]
	v_add_u32_e32 v32, s6, v90
	s_cmp_eq_u32 s26, 3
	v_lshl_add_u64 v[92:93], v[92:93], 0, s[74:75]
	s_waitcnt vmcnt(0)
	ds_write_b128 v32, v[80:83] offset:18432
	s_waitcnt lgkmcnt(0)
	s_barrier
	s_cbranch_scc1 .LBB0_1271
	v_mov_b32_e32 v103, v99
	s_branch .LBB0_1267
